# mLSTM Q.C: Q fragments read with conflict-free ds_read_b64 pairs instead of ds_read2_b64 (which banks mod 32 and conflicted 2-way on the 528-byte pitch)
# speedup vs baseline: 1.0037x; 1.0005x over previous
.Lml_no_v_fetch:
	ds_read_b128 v[72:75], v162
	ds_read_b128 v[76:79], v163 offset:33792
	ds_read_b128 v[84:87], v163 offset:42240
	ds_read_b128 v[210:213], v162 offset:64
	ds_read_b128 v[214:217], v163 offset:33856
	ds_read_b128 v[218:221], v163 offset:42304
	ds_read_b128 v[232:235], v162 offset:128
	ds_read_b128 v[236:239], v163 offset:33920
	ds_read_b128 v[240:243], v163 offset:42368
	ds_read_b128 v[176:179], v162 offset:192
	ds_read_b128 v[180:183], v163 offset:33984
	ds_read_b128 v[184:187], v163 offset:42432
	v_add_u32_e32 v167, 0x4000, v165
	v_add_u32_e32 v168, 0x6000, v165
	s_cmp_eq_u32 s88, 0x3e0000
	s_waitcnt lgkmcnt(10)
	v_mfma_f32_16x16x32_bf16 v[76:79], v[72:75], v[76:79], 0
	s_waitcnt lgkmcnt(9)
	v_mfma_f32_16x16x32_bf16 v[72:75], v[72:75], v[84:87], 0
	ds_read_b128 v[194:197], v162 offset:256
	ds_read_b128 v[198:201], v163 offset:34048
	ds_read_b128 v[202:205], v163 offset:42496
	s_waitcnt lgkmcnt(10)
	v_mfma_f32_16x16x32_bf16 v[76:79], v[210:213], v[214:217], v[76:79]
	s_waitcnt lgkmcnt(9)
	v_mfma_f32_16x16x32_bf16 v[72:75], v[210:213], v[218:221], v[72:75]
	ds_read_b128 v[210:213], v162 offset:320
	ds_read_b128 v[214:217], v163 offset:34112
	ds_read_b128 v[218:221], v163 offset:42560
	s_waitcnt lgkmcnt(10)
	v_mfma_f32_16x16x32_bf16 v[76:79], v[232:235], v[236:239], v[76:79]
	s_waitcnt lgkmcnt(9)
	v_mfma_f32_16x16x32_bf16 v[72:75], v[232:235], v[240:243], v[72:75]
	ds_read_b128 v[232:235], v162 offset:384
	ds_read_b128 v[236:239], v163 offset:34176
	ds_read_b128 v[240:243], v163 offset:42624
	s_waitcnt lgkmcnt(10)
	v_mfma_f32_16x16x32_bf16 v[76:79], v[176:179], v[180:183], v[76:79]
	s_waitcnt lgkmcnt(9)
	v_mfma_f32_16x16x32_bf16 v[72:75], v[176:179], v[184:187], v[72:75]
	ds_read_b128 v[176:179], v162 offset:448
	ds_read_b128 v[180:183], v163 offset:34240
	ds_read_b128 v[184:187], v163 offset:42688
	ds_read_b128 v[80:83], v150
	ds_read_b32 v0, v151
	ds_read_b32 v84, v164 offset:64
	s_waitcnt lgkmcnt(13)
	v_mfma_f32_16x16x32_bf16 v[76:79], v[194:197], v[198:201], v[76:79]
	s_waitcnt lgkmcnt(12)
	v_mfma_f32_16x16x32_bf16 v[72:75], v[194:197], v[202:205], v[72:75]
	s_waitcnt lgkmcnt(10)
	v_mfma_f32_16x16x32_bf16 v[76:79], v[210:213], v[214:217], v[76:79]
	s_waitcnt lgkmcnt(9)
	v_mfma_f32_16x16x32_bf16 v[72:75], v[210:213], v[218:221], v[72:75]
	s_waitcnt lgkmcnt(7)
	v_mfma_f32_16x16x32_bf16 v[76:79], v[232:235], v[236:239], v[76:79]
	s_waitcnt lgkmcnt(6)
	v_mfma_f32_16x16x32_bf16 v[72:75], v[232:235], v[240:243], v[72:75]
	s_waitcnt lgkmcnt(4)
	v_mfma_f32_16x16x32_bf16 v[76:79], v[176:179], v[180:183], v[76:79]
	s_waitcnt lgkmcnt(3)
	v_mfma_f32_16x16x32_bf16 v[72:75], v[176:179], v[184:187], v[72:75]
	s_nop 3
	s_waitcnt lgkmcnt(1)
	v_sub_f32_e32 v85, v0, v80
	v_min_f32_e32 v85, 0, v85
	s_waitcnt lgkmcnt(0)
	v_sub_f32_e32 v80, v84, v80
	v_exp_f32_e32 v85, v85
	v_min_f32_e32 v80, 0, v80
	v_exp_f32_e32 v80, v80
	v_mul_f32_e32 v76, v76, v85
	v_cndmask_b32_e64 v76, v76, 0, s[64:65]
	v_mul_f32_e32 v72, v72, v80
	v_cndmask_b32_e64 v72, v72, 0, s[66:67]
	v_cvt_pk_bf16_f32 v76, v76, v1
	v_add_u32_e32 v80, v155, v152
	ds_write_b16 v80, v76
	v_cvt_pk_bf16_f32 v72, v72, v1
	v_add_u32_e32 v76, v155, v153
	ds_write_b16 v76, v72
	v_sub_f32_e32 v72, v0, v81
	v_min_f32_e32 v72, 0, v72
	v_sub_f32_e32 v76, v84, v81
	v_exp_f32_e32 v72, v72
	v_min_f32_e32 v76, 0, v76
	v_exp_f32_e32 v76, v76
	v_mul_f32_e32 v72, v77, v72
	v_cndmask_b32_e64 v72, v72, 0, s[68:69]
	v_mul_f32_e32 v73, v73, v76
	v_cndmask_b32_e64 v73, v73, 0, s[70:71]
	v_cvt_pk_bf16_f32 v72, v72, v1
	v_add_u32_e32 v76, v156, v152
	ds_write_b16 v76, v72
	v_cvt_pk_bf16_f32 v72, v73, v1
	v_add_u32_e32 v73, v156, v153
	ds_write_b16 v73, v72
	v_sub_f32_e32 v72, v0, v82
	v_min_f32_e32 v72, 0, v72
	v_sub_f32_e32 v73, v84, v82
	v_exp_f32_e32 v72, v72
	v_min_f32_e32 v73, 0, v73
	v_exp_f32_e32 v73, v73
	v_sub_f32_e32 v0, v0, v83
	v_mul_f32_e32 v72, v78, v72
	v_cndmask_b32_e64 v72, v72, 0, s[72:73]
	v_mul_f32_e32 v73, v74, v73
	v_cndmask_b32_e64 v73, v73, 0, s[74:75]
	v_cvt_pk_bf16_f32 v72, v72, v1
	v_add_u32_e32 v74, v157, v152
	ds_write_b16 v74, v72
	v_cvt_pk_bf16_f32 v72, v73, v1
	v_add_u32_e32 v73, v157, v153
	ds_write_b16 v73, v72
	v_min_f32_e32 v0, 0, v0
	v_sub_f32_e32 v72, v84, v83
	v_exp_f32_e32 v0, v0
	v_min_f32_e32 v72, 0, v72
	v_exp_f32_e32 v72, v72
	v_add_u32_e32 v73, v158, v152
	v_mul_f32_e32 v0, v79, v0
	v_cndmask_b32_e64 v0, v0, 0, s[76:77]
	v_mul_f32_e32 v72, v75, v72
	v_cndmask_b32_e64 v72, v72, 0, s[78:79]
	v_cvt_pk_bf16_f32 v0, v0, v1
	ds_write_b16 v73, v0
	v_cvt_pk_bf16_f32 v0, v72, v1
	v_add_u32_e32 v72, v158, v153
	ds_write_b16 v72, v0
	v_add_u32_e32 v0, 0x2000, v165
	v_cvt_pk_bf16_f32 v72, v68, v69
	v_cvt_pk_bf16_f32 v73, v70, v71
	v_cvt_pk_bf16_f32 v74, v64, v65
	v_cvt_pk_bf16_f32 v75, v66, v67
	v_cvt_pk_bf16_f32 v206, v56, v57
	v_cvt_pk_bf16_f32 v207, v58, v59
	v_cvt_pk_bf16_f32 v208, v60, v61
	v_cvt_pk_bf16_f32 v209, v62, v63
	v_cvt_pk_bf16_f32 v222, v48, v49
	v_cvt_pk_bf16_f32 v223, v50, v51
	v_cvt_pk_bf16_f32 v224, v52, v53
	v_cvt_pk_bf16_f32 v225, v54, v55
	v_cvt_pk_bf16_f32 v226, v40, v41
	v_cvt_pk_bf16_f32 v227, v42, v43
	v_cvt_pk_bf16_f32 v228, v44, v45
	v_cvt_pk_bf16_f32 v229, v46, v47
	ds_read_b64 v[76:77], v165
	ds_read_b64 v[78:79], v165 offset:32
	ds_read_b64 v[80:81], v0 offset:256
	ds_read_b64 v[82:83], v0 offset:288
	ds_read_b64 v[84:85], v167 offset:512
	ds_read_b64 v[86:87], v167 offset:544
	ds_read_b64 v[88:89], v168 offset:768
	ds_read_b64 v[90:91], v168 offset:800
	ds_read_b64 v[176:177], v165 offset:64
	ds_read_b64 v[178:179], v165 offset:96
	ds_read_b64 v[180:181], v0 offset:320
	ds_read_b64 v[182:183], v0 offset:352
	s_waitcnt lgkmcnt(10)
	v_mfma_f32_16x16x32_bf16 v[76:79], v[76:79], v[72:75], 0
	ds_read_b64 v[184:185], v167 offset:576
	ds_read_b64 v[186:187], v167 offset:608
	s_waitcnt lgkmcnt(10)
	v_mfma_f32_16x16x32_bf16 v[80:83], v[80:83], v[72:75], 0
	ds_read_b64 v[194:195], v168 offset:832
	ds_read_b64 v[196:197], v168 offset:864
	s_waitcnt lgkmcnt(10)
	v_mfma_f32_16x16x32_bf16 v[84:87], v[84:87], v[72:75], 0
	ds_read_b64 v[198:199], v165 offset:128
	ds_read_b64 v[200:201], v165 offset:160
	s_waitcnt lgkmcnt(10)
	v_mfma_f32_16x16x32_bf16 v[88:91], v[88:91], v[72:75], 0
	ds_read_b64 v[202:203], v0 offset:384
	ds_read_b64 v[204:205], v0 offset:416
	s_waitcnt lgkmcnt(10)
	v_mfma_f32_16x16x32_bf16 v[76:79], v[176:179], v[206:209], v[76:79]
	ds_read_b64 v[210:211], v167 offset:640
	ds_read_b64 v[212:213], v167 offset:672
	s_waitcnt lgkmcnt(10)
	v_mfma_f32_16x16x32_bf16 v[80:83], v[180:183], v[206:209], v[80:83]
	ds_read_b64 v[214:215], v168 offset:896
	ds_read_b64 v[216:217], v168 offset:928
	s_waitcnt lgkmcnt(10)
	v_mfma_f32_16x16x32_bf16 v[84:87], v[184:187], v[206:209], v[84:87]
	ds_read_b64 v[232:233], v165 offset:192
	ds_read_b64 v[234:235], v165 offset:224
	s_waitcnt lgkmcnt(10)
	v_mfma_f32_16x16x32_bf16 v[88:91], v[194:197], v[206:209], v[88:91]
	ds_read_b64 v[236:237], v0 offset:448
	ds_read_b64 v[238:239], v0 offset:480
	s_waitcnt lgkmcnt(10)
	v_mfma_f32_16x16x32_bf16 v[76:79], v[198:201], v[222:225], v[76:79]
	ds_read_b64 v[240:241], v167 offset:704
	ds_read_b64 v[242:243], v167 offset:736
	s_waitcnt lgkmcnt(10)
	v_mfma_f32_16x16x32_bf16 v[80:83], v[202:205], v[222:225], v[80:83]
	ds_read_b64 v[244:245], v168 offset:960
	ds_read_b64 v[246:247], v168 offset:992
	s_waitcnt lgkmcnt(10)
	v_mfma_f32_16x16x32_bf16 v[84:87], v[210:213], v[222:225], v[84:87]
	s_waitcnt lgkmcnt(8)
	v_mfma_f32_16x16x32_bf16 v[88:91], v[214:217], v[222:225], v[88:91]
	s_waitcnt lgkmcnt(6)
	v_mfma_f32_16x16x32_bf16 v[76:79], v[232:235], v[226:229], v[76:79]
	s_waitcnt lgkmcnt(4)
	v_mfma_f32_16x16x32_bf16 v[80:83], v[236:239], v[226:229], v[80:83]
	s_waitcnt lgkmcnt(2)
	v_mfma_f32_16x16x32_bf16 v[84:87], v[240:243], v[226:229], v[84:87]
	s_waitcnt lgkmcnt(0)
	s_barrier
	v_mfma_f32_16x16x32_bf16 v[88:91], v[244:247], v[226:229], v[88:91]
